# attention passes: static s_setprio 1 for waves 4-7 during each pass; plus previous changes
# baseline (speedup 1.0000x reference)
; __device__ __forceinline__ unsigned cvt_pk_bf16(float lo, float hi) { unsigned r; asm volatile("v_cvt_pk_bf16_f32 %0, %1, %2" : "=v"(r) : "v"(lo), "v"(hi)); return r; }
; __device__ __forceinline__ float bf_lo(unsigned w) { return __uint_as_float(w << 16); }
; __device__ __forceinline__ float bf_hi(unsigned w) { return __uint_as_float(w & 0xffff0000u); }
;     __device__ __forceinline__ bf16_t* proj() const { return (bf16_t*)(ws + WS_PROJ); }
; #define AT_DMA_K(j, so) do { const char* _p = pb + (size_t)__builtin_amdgcn_readfirstlane(AT_ROW(j)) * (INW * 2); \
;         __builtin_amdgcn_global_load_lds((const unsigned*)(_p + dK), (LAS unsigned*)(lds + (so) + SHM_V + widu * 1024), 16, 0, 0); } while (0)
; template <bool ROBUST>
; __device__ __forceinline__ bool attn_pass(const bf16_t* __restrict__ proj, LAS char* lds, int qrow0, int ctxrow0, int latrow0, int NT, int h, int comp, f32x16 (&o)[4]) {
;     ...
;     { const bf16_t* Qw = proj + (size_t)(qrow0 + wid * 32 + r32) * INW + C_Q + h * 128 + comp * 64 + hi * 8;
; #pragma unroll
;       for (int d0 = 0; d0 < 4; ++d0) {
;           const u32x4 w = *(const u32x4*)(Qw + d0 * 16); constexpr float C = SCALE * 1.4426950408889634f; u32x4 s;
;           s.x = cvt_pk_bf16(bf_lo(w.x) * C, bf_hi(w.x) * C); s.y = cvt_pk_bf16(bf_lo(w.y) * C, bf_hi(w.y) * C); s.z = cvt_pk_bf16(bf_lo(w.z) * C, bf_hi(w.z) * C); s.w = cvt_pk_bf16(bf_lo(w.w) * C, bf_hi(w.w) * C);
;           qr[d0] = *reinterpret_cast<bf16x8*>(&s); } }
;     ...
;     const int widu = __builtin_amdgcn_readfirstlane(wid), l5 = lane >> 5, lp = lane & 31;
;     const int kv = wid * 8 + (lp >> 2);
;     const unsigned dV0 = (unsigned)((kv * INW + C_V + h * 128 + l5 * 32 + (lp & 3) * 8) * 2), dV1 = dV0 + 128u;
;     const int krow = wid * 8 + (lane >> 3);
;     const unsigned dK = (unsigned)((krow * INW + C_K + h * 128 + comp * 64) * 2 + (((lane & 7) ^ ((krow >> 1) & 7)) << 4));
;     ...
;     s16x4 dl0, dh0, dl1, dh1, dl2, dh2, dl3, dh3;
;     int sV = 0, sK = SLOT, sN = 2 * SLOT;
;     ...
;     const bool grpB = widu >= 4;
;     ...
;     AT_DMA_K(0, 0); AT_DMA_V(0, 0); AT_DMA_K(1, SLOT); AT_DMA_V(1, SLOT); AT_DMA_K(2, 2 * SLOT);
;     asm volatile("s_waitcnt vmcnt(4)" ::: "memory"); __syncthreads();
.LBB0_348:
	v_mov_b32_e32 v195, v0
	v_mov_b32_e32 v171, v147
	v_ashrrev_i32_e32 v8, 6, v195
	v_and_b32_e32 v194, 31, v195
	v_lshlrev_b32_e32 v2, 5, v8
	v_add3_u32 v2, v194, s30, v2
	v_ashrrev_i32_e32 v3, 31, v2
	v_lshlrev_b64 v[2:3], 13, v[2:3]
	v_bfe_u32 v4, v195, 5, 1
	v_lshl_add_u64 v[2:3], s[68:69], 0, v[2:3]
	v_lshl_add_u64 v[2:3], s[76:77], 1, v[2:3]
	v_lshlrev_b32_e32 v170, 4, v4
	v_lshl_add_u64 v[2:3], v[2:3], 0, v[170:171]
	global_load_dwordx4 v[48:51], v[2:3], off
	global_load_dwordx4 v[36:39], v[2:3], off offset:32
	global_load_dwordx4 v[40:43], v[2:3], off offset:64
	global_load_dwordx4 v[44:47], v[2:3], off offset:96
	v_lshlrev_b32_e32 v34, 3, v195
	s_ashr_i32 s67, s66, 31
	s_lshl_b64 s[24:25], s[66:67], 13
	v_readfirstlane_b32 s40, v8
	s_nop 3
	s_cmp_lt_u32 s40, 4
	s_cbranch_scc1 .Lat_prio_skip
	s_setprio 1
.Lat_prio_skip:
	s_add_u32 s8, s48, s24
	s_addc_u32 s9, s49, s25
	s_lshl_b32 s1, s40, 10
	s_add_i32 s78, s1, 0
	s_add_i32 s0, s78, 0x4000
	s_mov_b32 m0, s0
	v_mov_b32_e32 v173, v147
	s_add_i32 s79, s78, s1
	s_add_i32 s7, s79, 0x400
	v_cmp_eq_u32_e32 vcc, 0, v195
	v_lshlrev_b32_e32 v2, 3, v8
	v_bfe_u32 v3, v195, 2, 3
	v_or_b32_e32 v3, v2, v3
	v_and_b32_e32 v4, 32, v195
	v_lshl_or_b32 v3, v3, 12, v4
	v_and_b32_e32 v4, 24, v34
	v_or3_b32 v3, v3, v4, s31
	v_lshlrev_b32_e32 v172, 1, v3
	v_bfe_u32 v3, v195, 3, 3
	v_or_b32_e32 v2, v2, v3
	v_lshl_or_b32 v3, v2, 12, s31
	v_lshrrev_b32_e32 v2, 1, v2
	v_xor_b32_e32 v2, v2, v195
	v_lshlrev_b32_e32 v2, 4, v2
	v_or_b32_e32 v3, s76, v3
	v_and_b32_e32 v2, 0x70, v2
	v_lshl_or_b32 v146, v3, 1, v2
	v_lshl_add_u64 v[2:3], s[8:9], 0, v[146:147]
	v_lshl_add_u64 v[2:3], v[2:3], 0, s[10:11]
	global_load_lds_dwordx4 v[2:3], off
	v_lshl_add_u64 v[2:3], s[8:9], 0, v[172:173]
	v_lshl_add_u64 v[4:5], v[2:3], 0, s[38:39]
	s_mov_b32 m0, s79
	s_add_u32 s8, s8, 0x80000
	global_load_lds_dwordx4 v[4:5], off
	v_lshl_add_u64 v[2:3], v[2:3], 0, s[4:5]
	s_mov_b32 m0, s7
	s_addc_u32 s9, s9, 0
	global_load_lds_dwordx4 v[2:3], off
	v_lshl_add_u64 v[2:3], s[8:9], 0, v[146:147]
	s_add_i32 s42, s78, 0xa000
	v_lshl_add_u64 v[2:3], v[2:3], 0, s[10:11]
	s_mov_b32 m0, s42
	s_ashr_i32 s71, s70, 31
	global_load_lds_dwordx4 v[2:3], off
	v_lshl_add_u64 v[2:3], s[8:9], 0, v[172:173]
	s_add_i32 s1, s79, 0x6000
	s_add_i32 s2, s79, 0x6400
	s_lshl_b64 s[8:9], s[70:71], 13
	v_lshl_add_u64 v[4:5], v[2:3], 0, s[38:39]
	s_mov_b32 m0, s1
	s_add_u32 s8, s48, s8
	global_load_lds_dwordx4 v[4:5], off
	v_lshl_add_u64 v[2:3], v[2:3], 0, s[4:5]
	s_mov_b32 m0, s2
	s_addc_u32 s9, s49, s9
	global_load_lds_dwordx4 v[2:3], off
	v_lshl_add_u64 v[2:3], s[8:9], 0, v[146:147]
	s_add_i32 s80, s78, 0x10000
	v_lshl_add_u64 v[2:3], v[2:3], 0, s[10:11]
	s_mov_b32 m0, s80
	s_nop 0
	global_load_lds_dwordx4 v[2:3], off
	s_waitcnt vmcnt(10)
	v_lshlrev_b32_e32 v9, 16, v48
	v_and_b32_e32 v4, 0xffff0000, v48
	v_mul_f32_e32 v4, 0x3e38aa3b, v4
	v_mul_f32_e32 v9, 0x3e38aa3b, v9
	v_cvt_pk_bf16_f32 v148, v9, v4
	v_lshlrev_b32_e32 v4, 16, v49
	v_and_b32_e32 v5, 0xffff0000, v49
	v_mul_f32_e32 v4, 0x3e38aa3b, v4
	v_mul_f32_e32 v5, 0x3e38aa3b, v5
	v_cvt_pk_bf16_f32 v149, v4, v5
	v_lshlrev_b32_e32 v4, 16, v50
	v_and_b32_e32 v5, 0xffff0000, v50
	v_mul_f32_e32 v4, 0x3e38aa3b, v4
	v_mul_f32_e32 v5, 0x3e38aa3b, v5
	v_cvt_pk_bf16_f32 v150, v4, v5
	v_lshlrev_b32_e32 v4, 16, v51
	v_and_b32_e32 v5, 0xffff0000, v51
	v_mul_f32_e32 v4, 0x3e38aa3b, v4
	v_mul_f32_e32 v5, 0x3e38aa3b, v5
	v_cvt_pk_bf16_f32 v151, v4, v5
	s_waitcnt vmcnt(9)
	v_lshlrev_b32_e32 v9, 16, v36
	v_and_b32_e32 v4, 0xffff0000, v36
	v_mul_f32_e32 v4, 0x3e38aa3b, v4
	v_mul_f32_e32 v9, 0x3e38aa3b, v9
	v_cvt_pk_bf16_f32 v152, v9, v4
	v_lshlrev_b32_e32 v4, 16, v37
	v_and_b32_e32 v5, 0xffff0000, v37
	v_mul_f32_e32 v4, 0x3e38aa3b, v4
	v_mul_f32_e32 v5, 0x3e38aa3b, v5
	v_cvt_pk_bf16_f32 v153, v4, v5
	v_lshlrev_b32_e32 v4, 16, v38
	v_and_b32_e32 v5, 0xffff0000, v38
	v_mul_f32_e32 v4, 0x3e38aa3b, v4
	v_mul_f32_e32 v5, 0x3e38aa3b, v5
	v_cvt_pk_bf16_f32 v154, v4, v5
	v_lshlrev_b32_e32 v4, 16, v39
	v_and_b32_e32 v5, 0xffff0000, v39
	v_mul_f32_e32 v4, 0x3e38aa3b, v4
	v_mul_f32_e32 v5, 0x3e38aa3b, v5
	v_cvt_pk_bf16_f32 v155, v4, v5
	s_waitcnt vmcnt(8)
	v_lshlrev_b32_e32 v9, 16, v40
	v_and_b32_e32 v4, 0xffff0000, v40
	v_mul_f32_e32 v4, 0x3e38aa3b, v4
	v_mul_f32_e32 v9, 0x3e38aa3b, v9
	v_cvt_pk_bf16_f32 v156, v9, v4
	v_lshlrev_b32_e32 v4, 16, v41
	v_and_b32_e32 v5, 0xffff0000, v41
	v_mul_f32_e32 v4, 0x3e38aa3b, v4
	v_mul_f32_e32 v5, 0x3e38aa3b, v5
	v_cvt_pk_bf16_f32 v157, v4, v5
	v_lshlrev_b32_e32 v4, 16, v42
	v_and_b32_e32 v5, 0xffff0000, v42
	v_mul_f32_e32 v4, 0x3e38aa3b, v4
	v_mul_f32_e32 v5, 0x3e38aa3b, v5
	v_cvt_pk_bf16_f32 v158, v4, v5
	v_lshlrev_b32_e32 v4, 16, v43
	v_and_b32_e32 v5, 0xffff0000, v43
	v_mul_f32_e32 v4, 0x3e38aa3b, v4
	v_mul_f32_e32 v5, 0x3e38aa3b, v5
	v_cvt_pk_bf16_f32 v159, v4, v5
	s_waitcnt vmcnt(7)
	v_lshlrev_b32_e32 v9, 16, v44
	v_and_b32_e32 v4, 0xffff0000, v44
	v_mul_f32_e32 v4, 0x3e38aa3b, v4
	v_mul_f32_e32 v9, 0x3e38aa3b, v9
	v_cvt_pk_bf16_f32 v160, v9, v4
	v_lshlrev_b32_e32 v4, 16, v45
	v_and_b32_e32 v5, 0xffff0000, v45
	v_mul_f32_e32 v4, 0x3e38aa3b, v4
	v_mul_f32_e32 v5, 0x3e38aa3b, v5
	v_cvt_pk_bf16_f32 v161, v4, v5
	v_lshlrev_b32_e32 v4, 16, v46
	v_and_b32_e32 v5, 0xffff0000, v46
	v_mul_f32_e32 v4, 0x3e38aa3b, v4
	v_mul_f32_e32 v5, 0x3e38aa3b, v5
	v_cvt_pk_bf16_f32 v162, v4, v5
	v_lshlrev_b32_e32 v4, 16, v47
	v_and_b32_e32 v5, 0xffff0000, v47
	v_mul_f32_e32 v4, 0x3e38aa3b, v4
	v_mul_f32_e32 v5, 0x3e38aa3b, v5
	v_cvt_pk_bf16_f32 v163, v4, v5
	s_waitcnt vmcnt(4)
	s_waitcnt vmcnt(0) lgkmcnt(0)
	s_barrier
; #define LAS __attribute__((address_space(3)))
; __device__ __forceinline__ void qkt(f32x16& p0, f32x16& p1, const LAS char* Ks, const bf16x8* qr, int r32, int hi, float init) {
; #pragma unroll
;     for (int r = 0; r < 16; ++r) { p0[r] = init; p1[r] = init; }
; #pragma unroll
;     for (int d0 = 0; d0 < 4; ++d0) { const int cb = (d0 * 16 + hi * 8) * 2;
;         const bf16x8 b0 = *(const LAS bf16x8*)(Ks + AT_KSWZ(r32, cb));
;         const bf16x8 b1 = *(const LAS bf16x8*)(Ks + AT_KSWZ(32 + r32, cb));
;         p0 = __builtin_amdgcn_mfma_f32_32x32x16_bf16(b0, qr[d0], p0, 0, 0, 0);
;         p1 = __builtin_amdgcn_mfma_f32_32x32x16_bf16(b1, qr[d0], p1, 0, 0, 0); }
; }
; template <bool ROBUST>
; __device__ __forceinline__ bool attn_pass(const bf16_t* __restrict__ proj, LAS char* lds, int qrow0, int ctxrow0, int latrow0, int NT, int h, int comp, f32x16 (&o)[4]) {
;     ...
;     if (tid == 0) *(LAS int*)(lds + OFF_FLAG) = 0;
;     qkt(pA0, pA1, lds + SHM_V, qr, r32, hi, 0.f); partialSM<true>(pA0, pA1, m_reg, alA);
;     asm volatile("s_waitcnt vmcnt(1)" ::: "memory"); __syncthreads();
	s_and_saveexec_b64 s[8:9], vcc
	v_mov_b32_e32 v2, s16
	ds_write_b32 v2, v147
	s_or_b64 exec, exec, s[8:9]
	v_lshlrev_b32_e32 v35, 7, v194
	v_lshlrev_b32_e32 v2, 3, v194
	v_and_b32_e32 v48, 0x70, v2
	v_add_u32_e32 v49, 0, v35
	v_xad_u32 v6, v170, v48, v49
	ds_read_b128 v[2:5], v6 offset:16384
	ds_read_b128 v[6:9], v6 offset:20480
	v_or_b32_e32 v50, 32, v170
	v_xad_u32 v40, v50, v48, v49
	ds_read_b128 v[36:39], v40 offset:16384
	s_waitcnt lgkmcnt(2)
	v_mfma_f32_32x32x16_bf16 v[18:33], v[2:5], v[148:151], 0
	s_add_i32 s59, 0, 0x4000
	s_cmp_gt_i32 s40, 3
	v_or_b32_e32 v53, 64, v170
	s_cselect_b64 s[28:29], -1, 0
	s_cmp_lt_i32 s40, 4
	v_and_b32_e32 v52, 0x70, v34
	v_xad_u32 v34, v53, v48, v49
	s_waitcnt lgkmcnt(0)
	v_mfma_f32_32x32x16_bf16 v[18:33], v[36:39], v[152:155], v[18:33]
	ds_read_b128 v[40:43], v40 offset:20480
	ds_read_b128 v[44:47], v34 offset:16384
	s_cselect_b64 s[18:19], -1, 0
	s_lshl_b32 s8, s40, 11
	s_add_u32 s24, s48, s24
	v_add_u32_e32 v38, s59, v35
	v_or_b32_e32 v39, 0x60, v170
	s_addc_u32 s25, s49, s25
	v_xad_u32 v171, v170, v52, v38
	v_xad_u32 v199, v50, v52, v38
	v_xad_u32 v54, v39, v48, v49
	v_xad_u32 v200, v53, v52, v38
	v_xad_u32 v201, v39, v52, v38
	v_lshl_add_u64 v[38:39], s[24:25], 0, v[146:147]
	s_mov_b64 s[24:25], 0x180400
	s_mov_b32 m0, s0
	v_lshl_add_u64 v[38:39], v[38:39], 0, s[24:25]
	ds_read_b128 v[34:37], v34 offset:20480
	ds_read_b128 v[48:51], v54 offset:16384
	s_waitcnt lgkmcnt(2)
	v_mfma_f32_32x32x16_bf16 v[18:33], v[44:47], v[156:159], v[18:33]
	ds_read_b128 v[44:47], v54 offset:20480
	s_waitcnt vmcnt(1)
	s_waitcnt lgkmcnt(0)
	s_barrier
; template <bool FIRST>
; __device__ __forceinline__ void partialSM(f32x16& p0, f32x16& p1, float& m_reg, float& alpha) {
;     float pmax = p0[0];
; #pragma unroll
;     for (int r = 1; r < 16; ++r) pmax = fmaxf(pmax, p0[r]);
; #pragma unroll
;     for (int r = 0; r < 16; ++r) pmax = fmaxf(pmax, p1[r]);
;     { auto rr = __builtin_amdgcn_permlane32_swap(__float_as_uint(pmax), __float_as_uint(pmax), false, false);
;       pmax = fmaxf(__uint_as_float(rr[0]), __uint_as_float(rr[1])); }
;     if (!FIRST && __builtin_expect(__all(pmax <= THRL), 1)) { alpha = 1.f; }
;     else {
;         const float d = FIRST ? pmax : fmaxf(pmax, 0.f);
;         alpha = FIRST ? 1.f : __builtin_amdgcn_exp2f(-d); m_reg += d;
; #pragma unroll
;         for (int r = 0; r < 16; ++r) { p0[r] -= d; p1[r] -= d; }
;     }
; #pragma unroll
;     for (int r = 0; r < 16; ++r) p0[r] = __builtin_amdgcn_exp2f(p0[r]);
; }
	global_load_lds_dwordx4 v[38:39], off
	v_mfma_f32_32x32x16_bf16 v[2:17], v[6:9], v[148:151], 0
	v_add_u32_e32 v52, 0x6000, v199
	v_add_u32_e32 v53, 0x6000, v200
	v_add_u32_e32 v54, 0x6000, v201
	v_mfma_f32_32x32x16_bf16 v[2:17], v[40:43], v[152:155], v[2:17]
	v_add_u32_e32 v42, 0x6000, v171
	v_mfma_f32_32x32x16_bf16 v[18:33], v[48:51], v[160:163], v[18:33]
	v_mfma_f32_32x32x16_bf16 v[2:17], v[34:37], v[156:159], v[2:17]
	s_nop 10
	v_max_f32_e32 v48, v19, v19
	v_max_f32_e32 v49, v18, v18
	v_max_f32_e32 v38, v49, v48
	v_max3_f32 v34, v38, v20, v21
	v_max3_f32 v34, v34, v22, v23
	v_max3_f32 v34, v34, v24, v25
	v_max3_f32 v34, v34, v26, v27
	v_mfma_f32_32x32x16_bf16 v[2:17], v[44:47], v[160:163], v[2:17]
	v_max3_f32 v34, v34, v28, v29
	v_max3_f32 v34, v34, v30, v31
	v_max3_f32 v34, v34, v32, v33
	s_nop 8
	v_max3_f32 v34, v34, v2, v3
	v_max3_f32 v34, v34, v4, v5
	v_max3_f32 v34, v34, v6, v7
	v_max3_f32 v34, v34, v8, v9
	v_max3_f32 v34, v34, v10, v11
	v_max3_f32 v34, v34, v12, v13
	v_max3_f32 v34, v34, v14, v15
	v_max3_f32 v34, v34, v16, v17
	v_mov_b32_e32 v35, v34
	s_nop 1
	v_permlane32_swap_b32_e32 v34, v35
	v_max_f32_e32 v35, v35, v35
	v_max_f32_e32 v34, v34, v34
	v_max_f32_e32 v50, v34, v35
	ds_read_b128 v[34:37], v42 offset:0
	ds_read_b128 v[38:41], v42 offset:0x1000
	ds_read_b128 v[42:45], v52 offset:0
	ds_read_b128 v[46:49], v52 offset:0x1000
	ds_read_b128 v[68:71], v53 offset:0
	ds_read_b128 v[72:75], v53 offset:0x1000
	ds_read_b128 v[76:79], v54 offset:0
	ds_read_b128 v[114:117], v54 offset:0x1000
	v_add_f32_e32 v51, 0, v50
	v_sub_f32_e32 v18, v18, v50
	v_sub_f32_e32 v19, v19, v50
	v_sub_f32_e32 v20, v20, v50
	v_sub_f32_e32 v21, v21, v50
	v_sub_f32_e32 v22, v22, v50
	v_sub_f32_e32 v23, v23, v50
	v_sub_f32_e32 v24, v24, v50
	v_sub_f32_e32 v25, v25, v50
	v_sub_f32_e32 v26, v26, v50
	v_sub_f32_e32 v27, v27, v50
	v_sub_f32_e32 v28, v28, v50
	v_sub_f32_e32 v29, v29, v50
	v_sub_f32_e32 v30, v30, v50
	v_sub_f32_e32 v31, v31, v50
	v_sub_f32_e32 v32, v32, v50
	v_sub_f32_e32 v33, v33, v50
	v_exp_f32_e32 v18, v18
	v_exp_f32_e32 v19, v19
	v_exp_f32_e32 v20, v20
	v_exp_f32_e32 v21, v21
	v_exp_f32_e32 v22, v22
	v_exp_f32_e32 v23, v23
	v_exp_f32_e32 v24, v24
	v_exp_f32_e32 v25, v25
	v_exp_f32_e32 v26, v26
	v_exp_f32_e32 v27, v27
	v_exp_f32_e32 v28, v28
	v_exp_f32_e32 v29, v29
	v_exp_f32_e32 v30, v30
	v_exp_f32_e32 v31, v31
	v_exp_f32_e32 v32, v32
	v_exp_f32_e32 v33, v33
	v_xor_b32_e32 v66, 0x80000000, v51
	v_mov_b32_e32 v82, v66
	v_mov_b32_e32 v83, v66
	v_mov_b32_e32 v84, v66
	v_mov_b32_e32 v85, v66
	v_mov_b32_e32 v86, v66
	v_mov_b32_e32 v87, v66
	v_mov_b32_e32 v88, v66
	v_mov_b32_e32 v89, v66
	v_mov_b32_e32 v90, v66
	v_mov_b32_e32 v91, v66
	v_mov_b32_e32 v92, v66
	v_mov_b32_e32 v93, v66
	v_mov_b32_e32 v94, v66
	v_mov_b32_e32 v95, v66
	v_mov_b32_e32 v96, v66
	v_mov_b32_e32 v97, v66
	v_sub_f32_e32 v2, v2, v50
	v_sub_f32_e32 v3, v3, v50
	v_sub_f32_e32 v4, v4, v50
	v_sub_f32_e32 v5, v5, v50
	v_sub_f32_e32 v6, v6, v50
	v_sub_f32_e32 v7, v7, v50
	v_sub_f32_e32 v8, v8, v50
	v_sub_f32_e32 v9, v9, v50
	v_sub_f32_e32 v10, v10, v50
	v_sub_f32_e32 v11, v11, v50
	v_sub_f32_e32 v12, v12, v50
	v_sub_f32_e32 v13, v13, v50
	v_sub_f32_e32 v14, v14, v50
	v_sub_f32_e32 v15, v15, v50
	v_sub_f32_e32 v16, v16, v50
	v_sub_f32_e32 v17, v17, v50
	s_waitcnt lgkmcnt(6)
	s_waitcnt lgkmcnt(4)
	s_waitcnt lgkmcnt(2)
	v_exp_f32_e32 v2, v2
	v_mfma_f32_32x32x16_bf16 v[50:65], v[34:37], v[148:151], v[82:97]
	v_exp_f32_e32 v3, v3
	v_exp_f32_e32 v4, v4
	v_exp_f32_e32 v5, v5
	v_exp_f32_e32 v10, v10
	v_exp_f32_e32 v11, v11
	v_exp_f32_e32 v12, v12
	v_exp_f32_e32 v13, v13
	v_mfma_f32_32x32x16_bf16 v[98:113], v[38:41], v[148:151], v[82:97]
	v_exp_f32_e32 v6, v6
	v_exp_f32_e32 v7, v7
	v_exp_f32_e32 v14, v14
	v_exp_f32_e32 v15, v15
	v_exp_f32_e32 v8, v8
	v_exp_f32_e32 v9, v9
	v_exp_f32_e32 v16, v16
	v_mfma_f32_32x32x16_bf16 v[50:65], v[42:45], v[152:155], v[50:65]
	v_exp_f32_e32 v17, v17
	s_waitcnt lgkmcnt(0)
	v_pk_add_f32 v[34:35], v[18:19], v[20:21]
	v_pk_add_f32 v[36:37], v[26:27], v[28:29]
	v_pk_add_f32 v[38:39], v[4:5], v[2:3]
	v_pk_add_f32 v[40:41], v[12:13], v[10:11]
	v_pk_add_f32 v[34:35], v[34:35], v[22:23]
	v_mfma_f32_32x32x16_bf16 v[98:113], v[46:49], v[152:155], v[98:113]
	v_add_f32_e64 v36, v36, v30
	v_add_f32_e64 v37, v37, v31
	v_add_f32_e64 v38, v6, v38
	v_add_f32_e64 v39, v7, v39
	v_add_f32_e64 v40, v14, v40
	v_add_f32_e64 v41, v15, v41
	v_pk_add_f32 v[34:35], v[34:35], v[24:25]
	v_pk_add_f32 v[36:37], v[36:37], v[32:33]
	v_pk_add_f32 v[38:39], v[8:9], v[38:39]
	v_pk_add_f32 v[40:41], v[16:17], v[40:41]
	v_mfma_f32_32x32x16_bf16 v[50:65], v[68:71], v[156:159], v[50:65]
	v_add_f32_e64 v34, v34, v36
	v_add_f32_e64 v35, v35, v37
	v_add_f32_e64 v36, v38, v40
	v_add_f32_e64 v37, v39, v41
	v_add_f32_e64 v34, v36, v34
	v_add_f32_e64 v35, v37, v35
	v_pk_add_f32 v[174:175], v[34:35], v[34:35] op_sel:[0,1] op_sel_hi:[1,0]
	v_mfma_f32_32x32x16_bf16 v[98:113], v[72:75], v[156:159], v[98:113]
	v_mov_b32_e32 v175, v174
	s_nop 1
	v_permlane32_swap_b32_e32 v174, v175
	v_cvt_pk_bf16_f32 v72, v18, v19
	v_cvt_pk_bf16_f32 v73, v20, v21
	v_cvt_pk_bf16_f32 v74, v22, v23
	v_cvt_pk_bf16_f32 v75, v24, v25
	v_mfma_f32_32x32x16_bf16 v[50:65], v[76:79], v[160:163], v[50:65]
	v_cvt_pk_bf16_f32 v68, v26, v27
	v_cvt_pk_bf16_f32 v69, v28, v29
	v_cvt_pk_bf16_f32 v70, v30, v31
	v_cvt_pk_bf16_f32 v71, v32, v33
	v_cvt_pk_bf16_f32 v76, v2, v3
	v_cvt_pk_bf16_f32 v77, v4, v5
	v_cvt_pk_bf16_f32 v78, v6, v7
	v_mfma_f32_32x32x16_bf16 v[98:113], v[114:117], v[160:163], v[98:113]
	v_cvt_pk_bf16_f32 v79, v8, v9
	v_cvt_pk_bf16_f32 v114, v10, v11
	v_cvt_pk_bf16_f32 v115, v12, v13
	v_cvt_pk_bf16_f32 v116, v14, v15
	v_cvt_pk_bf16_f32 v117, v16, v17
	v_cndmask_b32_e64 v2, 0, 1, s[50:51]
	s_and_b64 vcc, exec, s[18:19]
	v_cmp_ne_u32_e64 s[44:45], 1, v2
	s_mov_b64 s[82:83], 0x100000
	s_cbranch_vccnz .LBB0_353
	s_lshl_b64 s[24:25], s[70:71], 13
	s_add_u32 s24, s48, s24
	s_addc_u32 s25, s49, s25
	v_lshl_add_u64 v[2:3], s[24:25], 0, v[172:173]
	s_add_i32 s9, s8, 0
	v_lshl_add_u64 v[4:5], v[2:3], 0, s[38:39]
	s_add_i32 m0, s9, 0xc000
	s_waitcnt vmcnt(1) lgkmcnt(0)
	s_barrier
	global_load_lds_dwordx4 v[4:5], off
	v_lshl_add_u64 v[2:3], v[2:3], 0, s[4:5]
	s_add_i32 m0, s9, 0xc400
	s_and_b64 vcc, exec, s[44:45]
	global_load_lds_dwordx4 v[2:3], off
	s_cbranch_vccnz .LBB0_353
	s_ashr_i32 s55, s54, 31
	s_lshl_b64 s[24:25], s[54:55], 13
	s_add_u32 s24, s48, s24
	s_addc_u32 s25, s49, s25
	v_lshl_add_u64 v[2:3], s[24:25], 0, v[146:147]
	v_lshl_add_u64 v[2:3], v[2:3], 0, s[10:11]
	s_mov_b32 m0, s42
	s_nop 0
	global_load_lds_dwordx4 v[2:3], off

; #define AT_PK4(P, BASE, OUT) do { u32x4 w = {cvt_pk_bf16(P[BASE + 0], P[BASE + 1]), cvt_pk_bf16(P[BASE + 2], P[BASE + 3]), cvt_pk_bf16(P[BASE + 4], P[BASE + 5]), cvt_pk_bf16(P[BASE + 6], P[BASE + 7])}; \
;     OUT = *reinterpret_cast<bf16x8*>(&w); } while (0)
; #define AT_TR8(D0, X) s16x4 X##l0 = tr_read<v_rd_off(D0, 0, 0)>(vb), X##h0 = tr_read<v_rd_off(D0, 0, 1)>(vb), X##l1 = tr_read<v_rd_off(D0, 1, 0)>(vb), X##h1 = tr_read<v_rd_off(D0, 1, 1)>(vb), \
;     X##l2 = tr_read<v_rd_off(D0, 2, 0)>(vb), X##h2 = tr_read<v_rd_off(D0, 2, 1)>(vb), X##l3 = tr_read<v_rd_off(D0, 3, 0)>(vb), X##h3 = tr_read<v_rd_off(D0, 3, 1)>(vb)
; #define AT_MF4(OD, X) do { OD = __builtin_amdgcn_mfma_f32_32x32x16_bf16(pa0, AT_PKV(X##l0, X##h0), OD, 0, 0, 0); OD = __builtin_amdgcn_mfma_f32_32x32x16_bf16(pa1, AT_PKV(X##l1, X##h1), OD, 0, 0, 0); \
;     OD = __builtin_amdgcn_mfma_f32_32x32x16_bf16(pa2, AT_PKV(X##l2, X##h2), OD, 0, 0, 0); OD = __builtin_amdgcn_mfma_f32_32x32x16_bf16(pa3, AT_PKV(X##l3, X##h3), OD, 0, 0, 0); } while (0)
; #define AT_W8(N, X) asm volatile("s_waitcnt lgkmcnt(" #N ")" : "+v"(X##l0), "+v"(X##h0), "+v"(X##l1), "+v"(X##h1), "+v"(X##l2), "+v"(X##h2), "+v"(X##l3), "+v"(X##h3) :: "memory")
; #define AT_W8(N, X) asm volatile("s_waitcnt lgkmcnt(" #N ")" : "+v"(X##l0), "+v"(X##h0), "+v"(X##l1), "+v"(X##h1), "+v"(X##l2), "+v"(X##h2), "+v"(X##l3), "+v"(X##h3) :: "memory")
; __device__ __forceinline__ void finishSM(f32x16& p0, f32x16& p1, float alpha, float& l_reg, bf16x8& pa0, bf16x8& pa1, bf16x8& pa2, bf16x8& pa3) {
; #pragma unroll
;     for (int r = 0; r < 16; ++r) p1[r] = __builtin_amdgcn_exp2f(p1[r]);
;     float ps = 0;
; #pragma unroll
;     for (int r = 0; r < 16; ++r) ps += p0[r];
; #pragma unroll
;     for (int r = 0; r < 16; ++r) ps += p1[r];
;     { auto rr = __builtin_amdgcn_permlane32_swap(__float_as_uint(ps), __float_as_uint(ps), false, false);
;       ps = __uint_as_float(rr[0]) + __uint_as_float(rr[1]); }
;     l_reg = l_reg * alpha + ps;
;     ...
;     AT_PK4(p0, 0, pa0); AT_PK4(p0, 8, pa1); AT_PK4(p1, 0, pa2); AT_PK4(p1, 8, pa3);
;     ...
; }
; __device__ __forceinline__ void pv_d0(f32x16* o, int vb, bf16x8 pa0, bf16x8 pa1, bf16x8 pa2, bf16x8 pa3) {
;     ...
;     AT_TR8(0, a); AT_TR8(1, b);
;     AT_W8(8, a); AT_TR8(2, c); AT_MF4(o[0], a);
;     AT_W8(8, b); AT_TR8(3, d); AT_MF4(o[1], b);
;     AT_W8(8, c); AT_MF4(o[2], c);
;     AT_W8(0, d); AT_MF4(o[3], d);
.LBB0_449:
	v_exp_f32_e32 v114, v98
	v_exp_f32_e32 v115, v99
	v_exp_f32_e32 v98, v100
	v_exp_f32_e32 v100, v101
	v_exp_f32_e32 v80, v102
	v_add_f32_e32 v67, 0, v114
	v_exp_f32_e32 v99, v103
	v_add_f32_e32 v67, v115, v67
	v_exp_f32_e32 v79, v104
	v_add_f32_e32 v67, v98, v67
	v_exp_f32_e32 v81, v105
	v_add_f32_e32 v67, v100, v67
	v_exp_f32_e32 v76, v106
	v_add_f32_e32 v67, v80, v67
	v_exp_f32_e32 v78, v107
	v_add_f32_e32 v67, v99, v67
	v_exp_f32_e32 v72, v108
	v_add_f32_e32 v67, v79, v67
	v_exp_f32_e32 v77, v109
	v_add_f32_e32 v67, v81, v67
	v_exp_f32_e32 v70, v110
	v_add_f32_e32 v67, v76, v67
	v_exp_f32_e32 v73, v111
	v_add_f32_e32 v67, v78, v67
	v_exp_f32_e32 v69, v112
	v_add_f32_e32 v67, v72, v67
	v_exp_f32_e32 v71, v113
	v_add_f32_e32 v67, v77, v67
	v_exp_f32_e32 v101, v82
	v_add_f32_e32 v67, v70, v67
	v_exp_f32_e32 v102, v83
	v_add_f32_e32 v67, v73, v67
	v_exp_f32_e32 v103, v84
	v_add_f32_e32 v67, v69, v67
	v_exp_f32_e32 v104, v85
	v_add_f32_e32 v67, v71, v67
	v_exp_f32_e32 v86, v86
	v_add_f32_e32 v67, v101, v67
	v_exp_f32_e32 v87, v87
	v_add_f32_e32 v67, v102, v67
	v_exp_f32_e32 v88, v88
	v_add_f32_e32 v67, v103, v67
	v_exp_f32_e32 v89, v89
	v_add_f32_e32 v67, v104, v67
	v_exp_f32_e32 v90, v90
	v_add_f32_e32 v67, v86, v67
	v_exp_f32_e32 v91, v91
	v_add_f32_e32 v67, v87, v67
	v_exp_f32_e32 v92, v92
	v_add_f32_e32 v67, v88, v67
	v_exp_f32_e32 v93, v93
	v_add_f32_e32 v67, v89, v67
	v_exp_f32_e32 v94, v94
	v_add_f32_e32 v67, v90, v67
	v_exp_f32_e32 v95, v95
	v_add_f32_e32 v67, v91, v67
	v_exp_f32_e32 v96, v96
	v_add_f32_e32 v67, v92, v67
	v_exp_f32_e32 v97, v97
	v_add_f32_e32 v67, v93, v67
	v_add_f32_e32 v67, v94, v67
	v_add_f32_e32 v67, v95, v67
	v_add_f32_e32 v67, v96, v67
	v_add_f32_e32 v67, v97, v67
	v_mov_b32_e32 v68, v67
	s_nop 1
	v_permlane32_swap_b32_e32 v67, v68
	v_cvt_pk_bf16_f32 v82, v114, v115
	v_cvt_pk_bf16_f32 v83, v98, v100
	v_cvt_pk_bf16_f32 v84, v80, v99
	v_cvt_pk_bf16_f32 v85, v79, v81
	v_cvt_pk_bf16_f32 v76, v76, v78
	v_cvt_pk_bf16_f32 v77, v72, v77
	v_cvt_pk_bf16_f32 v78, v70, v73
	v_cvt_pk_bf16_f32 v79, v69, v71
	v_cvt_pk_bf16_f32 v70, v101, v102
	v_cvt_pk_bf16_f32 v71, v103, v104
	v_cvt_pk_bf16_f32 v72, v86, v87
	v_cvt_pk_bf16_f32 v73, v88, v89
	v_cvt_pk_bf16_f32 v86, v90, v91
	v_cvt_pk_bf16_f32 v87, v92, v93
	v_cvt_pk_bf16_f32 v88, v94, v95
	v_cvt_pk_bf16_f32 v89, v96, v97
	s_nop 0
	v_permlane32_swap_b32_e32 v82, v84
	v_permlane32_swap_b32_e32 v83, v85
	v_permlane32_swap_b32_e32 v76, v78
	v_permlane32_swap_b32_e32 v77, v79
	v_permlane32_swap_b32_e32 v70, v72
	v_permlane32_swap_b32_e32 v71, v73
	v_permlane32_swap_b32_e32 v86, v88
	v_permlane32_swap_b32_e32 v87, v89
	ds_read_b64_tr_b16 v[90:91], v164 offset:0
	ds_read_b64_tr_b16 v[92:93], v164 offset:0x800
	ds_read_b64_tr_b16 v[94:95], v164 offset:0x1000
	ds_read_b64_tr_b16 v[96:97], v164 offset:0x1800
	ds_read_b64_tr_b16 v[98:99], v164 offset:0x2000
	ds_read_b64_tr_b16 v[100:101], v164 offset:0x2800
	ds_read_b64_tr_b16 v[102:103], v164 offset:0x3000
	ds_read_b64_tr_b16 v[104:105], v164 offset:0x3800
	ds_read_b64_tr_b16 v[106:107], v164 offset:0x200
	ds_read_b64_tr_b16 v[108:109], v164 offset:0xa00
	ds_read_b64_tr_b16 v[110:111], v164 offset:0x1200
	ds_read_b64_tr_b16 v[112:113], v164 offset:0x1a00
	ds_read_b64_tr_b16 v[114:115], v164 offset:0x2200
	ds_read_b64_tr_b16 v[116:117], v164 offset:0x2a00
	ds_read_b64_tr_b16 v[118:119], v164 offset:0x3200
	ds_read_b64_tr_b16 v[120:121], v164 offset:0x3a00
	s_nop 0
	s_waitcnt lgkmcnt(8)
	s_nop 0
	v_mfma_f32_32x32x16_bf16 v[50:65], v[82:85], v[90:93], v[50:65]
	ds_read_b64_tr_b16 v[90:91], v164 offset:0x400
	ds_read_b64_tr_b16 v[92:93], v164 offset:0xc00
	ds_read_b64_tr_b16 v[122:123], v164 offset:0x1400
	ds_read_b64_tr_b16 v[124:125], v164 offset:0x1c00
	ds_read_b64_tr_b16 v[126:127], v164 offset:0x2400
	ds_read_b64_tr_b16 v[128:129], v164 offset:0x2c00
	v_mfma_f32_32x32x16_bf16 v[50:65], v[76:79], v[94:97], v[50:65]
	ds_read_b64_tr_b16 v[94:95], v164 offset:0x3400
	ds_read_b64_tr_b16 v[96:97], v164 offset:0x3c00
	s_waitcnt lgkmcnt(8)
	v_mfma_f32_32x32x16_bf16 v[50:65], v[70:73], v[98:101], v[50:65]
	ds_read_b64_tr_b16 v[98:99], v164 offset:0x600
	ds_read_b64_tr_b16 v[100:101], v164 offset:0xe00
	v_mfma_f32_32x32x16_bf16 v[34:49], v[82:85], v[106:109], v[34:49]
	v_mfma_f32_32x32x16_bf16 v[50:65], v[86:89], v[102:105], v[50:65]
	ds_read_b64_tr_b16 v[102:103], v164 offset:0x1600
	ds_read_b64_tr_b16 v[104:105], v164 offset:0x1e00
	ds_read_b64_tr_b16 v[106:107], v164 offset:0x2600
	ds_read_b64_tr_b16 v[108:109], v164 offset:0x2e00
	v_mfma_f32_32x32x16_bf16 v[34:49], v[76:79], v[110:113], v[34:49]
	ds_read_b64_tr_b16 v[110:111], v164 offset:0x3600
	ds_read_b64_tr_b16 v[112:113], v164 offset:0x3e00
	s_waitcnt lgkmcnt(8)
	s_nop 0
	s_waitcnt lgkmcnt(0)
; #define LAS __attribute__((address_space(3)))
; __device__ __forceinline__ int crow(int r, int hi) { return (r & 3) + 8 * (r >> 2) + 4 * hi; }
; #define AT_TR8(D0, X) s16x4 X##l0 = tr_read<v_rd_off(D0, 0, 0)>(vb), X##h0 = tr_read<v_rd_off(D0, 0, 1)>(vb), X##l1 = tr_read<v_rd_off(D0, 1, 0)>(vb), X##h1 = tr_read<v_rd_off(D0, 1, 1)>(vb), \
;     X##l2 = tr_read<v_rd_off(D0, 2, 0)>(vb), X##h2 = tr_read<v_rd_off(D0, 2, 1)>(vb), X##l3 = tr_read<v_rd_off(D0, 3, 0)>(vb), X##h3 = tr_read<v_rd_off(D0, 3, 1)>(vb)
; #define AT_MF4(OD, X) do { OD = __builtin_amdgcn_mfma_f32_32x32x16_bf16(pa0, AT_PKV(X##l0, X##h0), OD, 0, 0, 0); OD = __builtin_amdgcn_mfma_f32_32x32x16_bf16(pa1, AT_PKV(X##l1, X##h1), OD, 0, 0, 0); \
;     OD = __builtin_amdgcn_mfma_f32_32x32x16_bf16(pa2, AT_PKV(X##l2, X##h2), OD, 0, 0, 0); OD = __builtin_amdgcn_mfma_f32_32x32x16_bf16(pa3, AT_PKV(X##l3, X##h3), OD, 0, 0, 0); } while (0)
; #define AT_W8(N, X) asm volatile("s_waitcnt lgkmcnt(" #N ")" : "+v"(X##l0), "+v"(X##h0), "+v"(X##l1), "+v"(X##h1), "+v"(X##l2), "+v"(X##h2), "+v"(X##l3), "+v"(X##h3) :: "memory")
; #define AT_W8(N, X) asm volatile("s_waitcnt lgkmcnt(" #N ")" : "+v"(X##l0), "+v"(X##h0), "+v"(X##l1), "+v"(X##h1), "+v"(X##l2), "+v"(X##h2), "+v"(X##l3), "+v"(X##h3) :: "memory")
; __device__ __forceinline__ void pv_d0(f32x16* o, int vb, bf16x8 pa0, bf16x8 pa1, bf16x8 pa2, bf16x8 pa3) {
;     ...
;     AT_TR8(0, a); AT_TR8(1, b);
;     AT_W8(8, a); AT_TR8(2, c); AT_MF4(o[0], a);
;     AT_W8(8, b); AT_TR8(3, d); AT_MF4(o[1], b);
;     AT_W8(8, c); AT_MF4(o[2], c);
;     AT_W8(0, d); AT_MF4(o[3], d);
; template <bool ROBUST>
; __device__ __forceinline__ bool attn_pass(const bf16_t* __restrict__ proj, LAS char* lds, int qrow0, int ctxrow0, int latrow0, int NT, int h, int comp, f32x16 (&o)[4]) {
;     ...
;     if (hi == 0) li_l[r32] = l_reg;
;     asm volatile("s_waitcnt lgkmcnt(0)" ::: "memory");
; #pragma unroll
;     for (int r = 0; r < 16; ++r) { const float rl = __builtin_amdgcn_rcpf(li_l[crow(r, hi)]);
; #pragma unroll
;         for (int d = 0; d < 4; ++d) o[d][r] *= rl; }
;     if constexpr (!ROBUST) { if (__any(any_ovf) && lane == 0) *(LAS int*)(lds + OFF_FLAG) = 1; }
;     __syncthreads();
	v_mfma_f32_32x32x16_bf16 v[18:33], v[82:85], v[90:93], v[18:33]
	v_mfma_f32_32x32x16_bf16 v[2:17], v[82:85], v[98:101], v[2:17]
	v_mfma_f32_32x32x16_bf16 v[18:33], v[76:79], v[122:125], v[18:33]
	v_mfma_f32_32x32x16_bf16 v[2:17], v[76:79], v[102:105], v[2:17]
	v_mfma_f32_32x32x16_bf16 v[34:49], v[70:73], v[114:117], v[34:49]
	v_mfma_f32_32x32x16_bf16 v[18:33], v[70:73], v[126:129], v[18:33]
	v_mfma_f32_32x32x16_bf16 v[2:17], v[70:73], v[106:109], v[2:17]
	v_mfma_f32_32x32x16_bf16 v[34:49], v[86:89], v[118:121], v[34:49]
	v_mfma_f32_32x32x16_bf16 v[18:33], v[86:89], v[94:97], v[18:33]
	v_mfma_f32_32x32x16_bf16 v[2:17], v[86:89], v[110:113], v[2:17]
	s_and_saveexec_b64 s[8:9], s[40:41]
	v_add_f32_e32 v69, v74, v75
	v_fmac_f32_e32 v69, v165, v179
	v_add_f32_e32 v67, v67, v68
	v_fmac_f32_e32 v67, v69, v66
	ds_write_b32 v163, v67
	s_or_b64 exec, exec, s[8:9]
	s_waitcnt lgkmcnt(0)
	v_add_u32_e32 v74, v162, v156
	ds_read_b128 v[66:69], v74
	ds_read_b128 v[70:73], v74 offset:32
	s_waitcnt lgkmcnt(1)
	v_rcp_f32_e32 v106, v66
	v_rcp_f32_e32 v107, v67
	v_rcp_f32_e32 v108, v68
	v_rcp_f32_e32 v109, v69
	ds_read_b128 v[66:69], v74 offset:64
	ds_read_b128 v[74:77], v74 offset:96
	s_waitcnt lgkmcnt(2)
	v_rcp_f32_e32 v110, v70
	v_rcp_f32_e32 v111, v71
	v_rcp_f32_e32 v112, v72
	v_rcp_f32_e32 v113, v73
	s_waitcnt lgkmcnt(1)
	v_rcp_f32_e32 v114, v66
	v_rcp_f32_e32 v116, v68
	s_waitcnt lgkmcnt(0)
	v_rcp_f32_e32 v118, v74
	v_rcp_f32_e32 v120, v76
	v_rcp_f32_e32 v121, v77
	v_rcp_f32_e32 v119, v75
	v_rcp_f32_e32 v117, v69
	v_rcp_f32_e32 v115, v67
	v_pk_mul_f32 v[70:71], v[64:65], v[120:121]
	v_pk_mul_f32 v[72:73], v[62:63], v[118:119]
	v_pk_mul_f32 v[76:77], v[60:61], v[116:117]
	v_pk_mul_f32 v[80:81], v[58:59], v[114:115]
	v_pk_mul_f32 v[84:85], v[56:57], v[112:113]
	v_pk_mul_f32 v[88:89], v[54:55], v[110:111]
	v_pk_mul_f32 v[92:93], v[52:53], v[108:109]
	v_pk_mul_f32 v[98:99], v[50:51], v[106:107]
	v_pk_mul_f32 v[82:83], v[48:49], v[120:121]
	v_pk_mul_f32 v[86:87], v[46:47], v[118:119]
	v_pk_mul_f32 v[90:91], v[44:45], v[116:117]
	v_pk_mul_f32 v[94:95], v[42:43], v[114:115]
	v_pk_mul_f32 v[96:97], v[40:41], v[112:113]
	v_pk_mul_f32 v[100:101], v[38:39], v[110:111]
	v_pk_mul_f32 v[102:103], v[36:37], v[108:109]
	v_pk_mul_f32 v[104:105], v[34:35], v[106:107]
	v_pk_mul_f32 v[66:67], v[32:33], v[120:121]
	v_pk_mul_f32 v[68:69], v[30:31], v[118:119]
	v_pk_mul_f32 v[74:75], v[28:29], v[116:117]
	v_pk_mul_f32 v[78:79], v[26:27], v[114:115]
	v_pk_mul_f32 v[46:47], v[24:25], v[112:113]
	v_pk_mul_f32 v[28:29], v[22:23], v[110:111]
	v_pk_mul_f32 v[24:25], v[20:21], v[108:109]
	v_pk_mul_f32 v[18:19], v[18:19], v[106:107]
	v_pk_mul_f32 v[64:65], v[16:17], v[120:121]
	v_pk_mul_f32 v[62:63], v[14:15], v[118:119]
	v_pk_mul_f32 v[60:61], v[12:13], v[116:117]
	v_pk_mul_f32 v[58:59], v[10:11], v[114:115]
	v_pk_mul_f32 v[38:39], v[8:9], v[112:113]
	v_pk_mul_f32 v[34:35], v[6:7], v[110:111]
	v_pk_mul_f32 v[54:55], v[4:5], v[108:109]
	v_pk_mul_f32 v[10:11], v[2:3], v[106:107]
	s_barrier
	s_setprio 0
	s_andn2_b64 vcc, exec, s[72:73]
	s_mov_b64 s[8:9], -1
	s_cbranch_vccnz .LBB0_347
	s_branch .LBB0_453
.LBB0_452:
	v_rcp_f32_e32 v106, v78
	v_rcp_f32_e32 v107, v79
	v_rcp_f32_e32 v108, v80
	v_rcp_f32_e32 v109, v81
	v_rcp_f32_e32 v110, v74
	v_rcp_f32_e32 v111, v75
	v_rcp_f32_e32 v112, v76
	v_rcp_f32_e32 v113, v77
	v_rcp_f32_e32 v114, v66
	v_rcp_f32_e32 v116, v68
	v_rcp_f32_e32 v118, v70
	v_rcp_f32_e32 v120, v72
	v_rcp_f32_e32 v121, v73
	v_rcp_f32_e32 v119, v71
	v_rcp_f32_e32 v117, v69
	v_rcp_f32_e32 v115, v67
	v_pk_mul_f32 v[70:71], v[16:17], v[120:121]
	v_pk_mul_f32 v[72:73], v[14:15], v[118:119]
	v_pk_mul_f32 v[76:77], v[12:13], v[116:117]
	v_pk_mul_f32 v[80:81], v[10:11], v[114:115]
	v_pk_mul_f32 v[84:85], v[8:9], v[112:113]
	v_pk_mul_f32 v[88:89], v[6:7], v[110:111]
	v_pk_mul_f32 v[92:93], v[4:5], v[108:109]
	v_pk_mul_f32 v[98:99], v[2:3], v[106:107]
	v_pk_mul_f32 v[82:83], v[32:33], v[120:121]
	v_pk_mul_f32 v[86:87], v[30:31], v[118:119]
	v_pk_mul_f32 v[90:91], v[28:29], v[116:117]
	v_pk_mul_f32 v[94:95], v[26:27], v[114:115]
	v_pk_mul_f32 v[96:97], v[24:25], v[112:113]
	v_pk_mul_f32 v[100:101], v[22:23], v[110:111]
	v_pk_mul_f32 v[102:103], v[20:21], v[108:109]
	v_pk_mul_f32 v[104:105], v[18:19], v[106:107]
	v_pk_mul_f32 v[66:67], v[48:49], v[120:121]
	v_pk_mul_f32 v[68:69], v[46:47], v[118:119]
	v_pk_mul_f32 v[74:75], v[44:45], v[116:117]
	v_pk_mul_f32 v[78:79], v[42:43], v[114:115]
	v_pk_mul_f32 v[46:47], v[40:41], v[112:113]
	v_pk_mul_f32 v[28:29], v[38:39], v[110:111]
	v_pk_mul_f32 v[24:25], v[36:37], v[108:109]
	v_pk_mul_f32 v[18:19], v[34:35], v[106:107]
	v_pk_mul_f32 v[64:65], v[64:65], v[120:121]
	v_pk_mul_f32 v[62:63], v[62:63], v[118:119]
	v_pk_mul_f32 v[60:61], v[60:61], v[116:117]
	v_pk_mul_f32 v[58:59], v[58:59], v[114:115]
	v_pk_mul_f32 v[38:39], v[56:57], v[112:113]
	v_pk_mul_f32 v[34:35], v[54:55], v[110:111]
	v_pk_mul_f32 v[54:55], v[52:53], v[108:109]
	v_pk_mul_f32 v[10:11], v[50:51], v[106:107]
	s_mov_b64 s[90:91], s[26:27]
	s_setprio 0
	s_andn2_b64 vcc, exec, s[72:73]
	s_mov_b64 s[8:9], -1
	s_cbranch_vccnz .LBB0_347
